# DPP row ops and permlane swaps replace ds_bpermute round trips: norm1 sum of squares, norm2 router reduce-scatter and softmax (bit-identical logits)
# baseline (speedup 1.0000x reference)
.LBB0_331:
	s_waitcnt vmcnt(3)
	v_pk_mul_f32 v[64:65], v[14:15], v[14:15]
	s_waitcnt vmcnt(2)
	v_pk_mul_f32 v[66:67], v[10:11], v[10:11]
	v_pk_mul_f32 v[58:59], v[16:17], v[16:17]
	v_pk_mul_f32 v[62:63], v[12:13], v[12:13]
	v_mov_b32_e32 v68, v64
	v_mov_b32_e32 v69, v66
	v_mov_b32_e32 v66, v65
	v_pk_add_f32 v[64:65], v[68:69], v[66:67]
	v_mov_b32_e32 v66, v58
	v_mov_b32_e32 v67, v62
	s_waitcnt vmcnt(0)
	v_pk_mul_f32 v[54:55], v[2:3], v[2:3]
	v_pk_mul_f32 v[56:57], v[6:7], v[6:7]
	v_pk_add_f32 v[64:65], v[66:67], v[64:65]
	v_mov_b32_e32 v62, v59
	v_pk_mul_f32 v[50:51], v[4:5], v[4:5]
	v_pk_mul_f32 v[52:53], v[8:9], v[8:9]
	v_pk_add_f32 v[58:59], v[62:63], v[64:65]
	v_mov_b32_e32 v62, v54
	v_mov_b32_e32 v63, v56
	v_mov_b32_e32 v56, v55
	v_pk_add_f32 v[54:55], v[62:63], v[56:57]
	v_mov_b32_e32 v56, v50
	v_mov_b32_e32 v57, v52
	v_pk_add_f32 v[54:55], v[56:57], v[54:55]
	v_mov_b32_e32 v52, v51
	v_pk_add_f32 v[50:51], v[52:53], v[54:55]
	v_add_f32_e32 v37, v58, v59
	v_add_f32_e32 v37, v51, v37
	v_add_f32_e32 v37, v50, v37
	v_lshlrev_b64 v[62:63], 10, v[40:41]
	v_lshlrev_b64 v[40:41], 11, v[40:41]
	v_add_f32_dpp v37, v37, v37 quad_perm:[1,0,3,2] row_mask:0xf bank_mask:0xf
	v_cvt_pk_bf16_f32 v52, v14, v15
	v_cvt_pk_bf16_f32 v53, v16, v17
	v_add_f32_dpp v37, v37, v37 quad_perm:[2,3,0,1] row_mask:0xf bank_mask:0xf
	v_lshl_add_u64 v[64:65], v[22:23], 0, v[40:41]
	global_store_dwordx2 v[64:65], v[52:53], off
	v_add_f32_dpp v37, v37, v37 row_half_mirror row_mask:0xf bank_mask:0xf
	ds_read_b128 v[52:55], v73 offset:8192
	ds_read_b128 v[56:59], v73 offset:12288
	v_add_f32_dpp v37, v37, v37 row_mirror row_mask:0xf bank_mask:0xf
	s_nop 1
	v_add_f32_dpp v37, v37, v37 row_bcast:15 row_mask:0xa bank_mask:0xf
	s_nop 1
	v_add_f32_dpp v37, v37, v37 row_bcast:31 row_mask:0xc bank_mask:0xf
	s_nop 0
	v_readlane_b32 s100, v37, 63
	s_nop 1
	v_mov_b32_e32 v37, s100
	s_waitcnt lgkmcnt(0)
	v_fmamk_f32 v37, v37, 0x3a800000, v176
	v_cmp_gt_f32_e32 vcc, s25, v37
	v_mul_f32_e32 v39, 0x4b800000, v37
	s_nop 0
	v_cndmask_b32_e32 v37, v37, v39, vcc
	v_rsq_f32_e32 v37, v37
	s_nop 0
	v_mul_f32_e32 v39, 0x45800000, v37
	v_cndmask_b32_e32 v50, v37, v39, vcc
	v_pk_mul_f32 v[14:15], v[14:15], v[50:51] op_sel_hi:[1,0]
	v_mov_b32_e32 v37, v131
	v_pk_fma_f32 v[14:15], v[52:53], v[14:15], v[56:57]
	v_pk_mul_f32 v[16:17], v[16:17], v[50:51] op_sel_hi:[1,0]
	v_cvt_pk_bf16_f32 v52, v14, v15
	v_med3_f32 v14, v14, s26, v209
	v_med3_f32 v15, v15, s26, v209
	v_cvt_pk_fp8_f32 v37, v14, v15
	v_pk_fma_f32 v[54:55], v[54:55], v[16:17], v[58:59]
	v_lshl_add_u64 v[16:17], v[30:31], 0, v[40:41]
	v_med3_f32 v14, v54, s26, v209
	v_med3_f32 v15, v55, s26, v209
	v_cvt_pk_fp8_f32 v37, v14, v15 op_sel:[0,0,1]
	v_cvt_pk_bf16_f32 v53, v54, v55
	v_lshl_add_u64 v[14:15], v[32:33], 0, v[62:63]
	v_cvt_pk_bf16_f32 v40, v10, v11
	v_cvt_pk_bf16_f32 v41, v12, v13
	global_store_dwordx2 v[16:17], v[52:53], off
	global_store_dword v[14:15], v37, off
	global_store_dwordx2 v[64:65], v[40:41], off offset:512
	ds_read_b128 v[52:55], v73 offset:9216
	ds_read_b128 v[56:59], v73 offset:13312
	v_pk_mul_f32 v[10:11], v[10:11], v[50:51] op_sel_hi:[1,0]
	v_mov_b32_e32 v37, v131
	v_pk_mul_f32 v[12:13], v[12:13], v[50:51] op_sel_hi:[1,0]
	v_cmp_le_i32_e32 vcc, s2, v60
	s_waitcnt lgkmcnt(0)
	v_pk_fma_f32 v[10:11], v[52:53], v[10:11], v[56:57]
	v_pk_fma_f32 v[12:13], v[54:55], v[12:13], v[58:59]
	v_cvt_pk_bf16_f32 v40, v10, v11
	v_med3_f32 v10, v10, s26, v209
	v_med3_f32 v11, v11, s26, v209
	v_cvt_pk_fp8_f32 v37, v10, v11
	v_med3_f32 v10, v12, s26, v209
	v_med3_f32 v11, v13, s26, v209
	v_cvt_pk_bf16_f32 v41, v12, v13
	v_cvt_pk_fp8_f32 v37, v10, v11 op_sel:[0,0,1]
	v_cvt_pk_bf16_f32 v10, v6, v7
	v_cvt_pk_bf16_f32 v11, v8, v9
	global_store_dwordx2 v[16:17], v[40:41], off offset:512
	global_store_dword v[14:15], v37, off offset:256
	global_store_dwordx2 v[64:65], v[10:11], off offset:1024
	ds_read_b128 v[10:13], v73 offset:10240
	ds_read_b128 v[52:55], v73 offset:14336
	v_pk_mul_f32 v[6:7], v[6:7], v[50:51] op_sel_hi:[1,0]
	v_pk_mul_f32 v[8:9], v[8:9], v[50:51] op_sel_hi:[1,0]
	s_or_b64 s[70:71], vcc, s[70:71]
	v_mov_b64_e32 v[56:57], v[48:49]
	s_waitcnt lgkmcnt(0)
	v_pk_fma_f32 v[8:9], v[8:9], v[12:13], v[54:55]
	v_pk_fma_f32 v[6:7], v[6:7], v[10:11], v[52:53]
	v_cvt_pk_bf16_f32 v11, v8, v9
	v_cvt_pk_bf16_f32 v10, v6, v7
	global_store_dwordx2 v[16:17], v[10:11], off offset:1024
	v_med3_f32 v6, v6, s26, v209
	v_med3_f32 v7, v7, s26, v209
	v_mov_b32_e32 v10, v131
	v_cvt_pk_fp8_f32 v10, v6, v7
	v_med3_f32 v6, v8, s26, v209
	v_med3_f32 v7, v9, s26, v209
	v_mov_b64_e32 v[52:53], v[44:45]
	v_cvt_pk_fp8_f32 v10, v6, v7 op_sel:[0,0,1]
	v_cvt_pk_bf16_f32 v6, v2, v3
	v_cvt_pk_bf16_f32 v7, v4, v5
	v_pk_mul_f32 v[2:3], v[2:3], v[50:51] op_sel_hi:[1,0]
	global_store_dword v[14:15], v10, off offset:512
	global_store_dwordx2 v[64:65], v[6:7], off offset:1536
	ds_read_b128 v[6:9], v73 offset:11264
	ds_read_b128 v[10:13], v73 offset:15360
	v_pk_mul_f32 v[4:5], v[4:5], v[50:51] op_sel_hi:[1,0]
	v_mov_b64_e32 v[50:51], v[42:43]
	v_mov_b64_e32 v[54:55], v[46:47]
	v_mov_b32_e32 v37, v61
	s_waitcnt lgkmcnt(0)
	v_pk_fma_f32 v[4:5], v[4:5], v[8:9], v[12:13]
	v_pk_fma_f32 v[2:3], v[2:3], v[6:7], v[10:11]
	v_cvt_pk_bf16_f32 v7, v4, v5
	v_cvt_pk_bf16_f32 v6, v2, v3
	global_store_dwordx2 v[16:17], v[6:7], off offset:1536
	v_med3_f32 v2, v2, s26, v209
	v_med3_f32 v3, v3, s26, v209
	v_mov_b32_e32 v6, v131
	v_cvt_pk_fp8_f32 v6, v2, v3
	v_med3_f32 v2, v4, s26, v209
	v_med3_f32 v3, v5, s26, v209
	v_mov_b32_e32 v39, v72
	v_cvt_pk_fp8_f32 v6, v2, v3 op_sel:[0,0,1]
	v_mov_b32_e32 v40, v60
	global_store_dword v[14:15], v6, off offset:768
	s_andn2_b64 exec, exec, s[70:71]
	s_cbranch_execz .LBB0_306

.LBB0_1261:
	s_or_b64 exec, exec, s[16:17]
	v_lshlrev_b32_e32 v109, 16, v102
	v_lshlrev_b32_e32 v108, 16, v106
	v_lshlrev_b32_e32 v111, 16, v100
	v_lshlrev_b32_e32 v110, 16, v104
	s_waitcnt lgkmcnt(3)
	v_pk_fma_f32 v[112:113], v[14:15], v[110:111], v[108:109] op_sel_hi:[0,1,1]
	v_and_b32_e32 v109, 0xffff0000, v102
	v_and_b32_e32 v108, 0xffff0000, v106
	v_and_b32_e32 v111, 0xffff0000, v100
	v_and_b32_e32 v110, 0xffff0000, v104
	v_pk_fma_f32 v[116:117], v[14:15], v[110:111], v[108:109] op_sel:[1,0,0]
	v_lshlrev_b32_e32 v15, 16, v103
	v_lshlrev_b32_e32 v14, 16, v107
	v_lshlrev_b32_e32 v109, 16, v101
	v_lshlrev_b32_e32 v108, 16, v105
	v_pk_fma_f32 v[140:141], v[16:17], v[108:109], v[14:15] op_sel_hi:[0,1,1]
	v_and_b32_e32 v15, 0xffff0000, v103
	v_and_b32_e32 v14, 0xffff0000, v107
	v_and_b32_e32 v101, 0xffff0000, v101
	v_and_b32_e32 v100, 0xffff0000, v105
	v_mov_b32_e32 v16, v17
	v_pk_fma_f32 v[16:17], v[16:17], v[100:101], v[14:15] op_sel_hi:[0,1,1]
	v_pk_mul_f32 v[14:15], v[116:117], v[116:117]
	v_lshlrev_b32_e32 v101, 16, v92
	v_pk_fma_f32 v[14:15], v[112:113], v[112:113], v[14:15]
	v_lshlrev_b32_e32 v100, 16, v96
	v_pk_fma_f32 v[14:15], v[140:141], v[140:141], v[14:15]
	s_mov_b32 s16, 0x3a800000
	v_pk_fma_f32 v[104:105], v[16:17], v[16:17], v[14:15]
	v_lshlrev_b32_e32 v15, 16, v94
	v_lshlrev_b32_e32 v14, 16, v98
	s_waitcnt lgkmcnt(2)
	v_pk_fma_f32 v[102:103], v[10:11], v[100:101], v[14:15] op_sel_hi:[0,1,1]
	v_and_b32_e32 v15, 0xffff0000, v94
	v_and_b32_e32 v14, 0xffff0000, v98
	v_and_b32_e32 v101, 0xffff0000, v92
	v_and_b32_e32 v100, 0xffff0000, v96
	v_pk_fma_f32 v[106:107], v[10:11], v[100:101], v[14:15] op_sel:[1,0,0]
	v_lshlrev_b32_e32 v11, 16, v95
	v_lshlrev_b32_e32 v10, 16, v99
	v_lshlrev_b32_e32 v15, 16, v93
	v_lshlrev_b32_e32 v14, 16, v97
	v_pk_fma_f32 v[108:109], v[12:13], v[14:15], v[10:11] op_sel_hi:[0,1,1]
	v_and_b32_e32 v11, 0xffff0000, v95
	v_and_b32_e32 v10, 0xffff0000, v99
	v_and_b32_e32 v15, 0xffff0000, v93
	v_and_b32_e32 v14, 0xffff0000, v97
	v_mov_b32_e32 v12, v13
	v_pk_fma_f32 v[110:111], v[12:13], v[14:15], v[10:11] op_sel_hi:[0,1,1]
	v_pk_mul_f32 v[10:11], v[106:107], v[106:107]
	v_lshlrev_b32_e32 v13, 16, v84
	v_pk_fma_f32 v[10:11], v[102:103], v[102:103], v[10:11]
	v_lshlrev_b32_e32 v12, 16, v88
	v_pk_fma_f32 v[10:11], v[108:109], v[108:109], v[10:11]
	v_and_b32_e32 v15, 0xffff0000, v84
	v_pk_fma_f32 v[94:95], v[110:111], v[110:111], v[10:11]
	v_lshlrev_b32_e32 v11, 16, v86
	v_lshlrev_b32_e32 v10, 16, v90
	s_waitcnt lgkmcnt(1)
	v_pk_fma_f32 v[10:11], v[6:7], v[12:13], v[10:11] op_sel_hi:[0,1,1]
	v_and_b32_e32 v13, 0xffff0000, v86
	v_and_b32_e32 v12, 0xffff0000, v90
	v_and_b32_e32 v14, 0xffff0000, v88
	v_pk_fma_f32 v[12:13], v[6:7], v[14:15], v[12:13] op_sel:[1,0,0]
	v_lshlrev_b32_e32 v7, 16, v87
	v_lshlrev_b32_e32 v6, 16, v91
	v_lshlrev_b32_e32 v15, 16, v85
	v_lshlrev_b32_e32 v14, 16, v89
	v_pk_fma_f32 v[98:99], v[8:9], v[14:15], v[6:7] op_sel_hi:[0,1,1]
	v_pk_mul_f32 v[6:7], v[12:13], v[12:13]
	v_and_b32_e32 v15, 0xffff0000, v85
	v_pk_fma_f32 v[6:7], v[10:11], v[10:11], v[6:7]
	v_and_b32_e32 v14, 0xffff0000, v89
	v_pk_fma_f32 v[96:97], v[98:99], v[98:99], v[6:7]
	v_and_b32_e32 v7, 0xffff0000, v87
	v_and_b32_e32 v6, 0xffff0000, v91
	v_mov_b32_e32 v8, v9
	v_pk_fma_f32 v[100:101], v[8:9], v[14:15], v[6:7] op_sel_hi:[0,1,1]
	v_and_b32_e32 v7, 0xffff0000, v79
	v_and_b32_e32 v6, 0xffff0000, v83
	v_and_b32_e32 v9, 0xffff0000, v77
	v_and_b32_e32 v8, 0xffff0000, v81
	s_waitcnt lgkmcnt(0)
	v_mov_b32_e32 v14, v5
	v_pk_fma_f32 v[6:7], v[14:15], v[8:9], v[6:7] op_sel_hi:[0,1,1]
	v_lshlrev_b32_e32 v9, 16, v78
	v_lshlrev_b32_e32 v8, 16, v82
	v_lshlrev_b32_e32 v15, 16, v76
	v_lshlrev_b32_e32 v14, 16, v80
	v_pk_fma_f32 v[14:15], v[2:3], v[14:15], v[8:9] op_sel_hi:[0,1,1]
	v_and_b32_e32 v9, 0xffff0000, v78
	v_and_b32_e32 v8, 0xffff0000, v82
	v_and_b32_e32 v85, 0xffff0000, v76
	v_and_b32_e32 v84, 0xffff0000, v80
	v_pk_fma_f32 v[90:91], v[2:3], v[84:85], v[8:9] op_sel:[1,0,0]
	v_lshlrev_b32_e32 v9, 16, v79
	v_pk_mul_f32 v[2:3], v[90:91], v[90:91]
	v_lshlrev_b32_e32 v8, 16, v83
	v_lshlrev_b32_e32 v77, 16, v77
	v_lshlrev_b32_e32 v76, 16, v81
	v_pk_fma_f32 v[2:3], v[14:15], v[14:15], v[2:3]
	v_pk_fma_f32 v[92:93], v[4:5], v[76:77], v[8:9] op_sel_hi:[0,1,1]
	v_pk_add_f32 v[4:5], v[104:105], v[94:95]
	v_pk_fma_f32 v[8:9], v[100:101], v[100:101], v[96:97]
	v_pk_fma_f32 v[2:3], v[92:93], v[92:93], v[2:3]
	v_pk_add_f32 v[4:5], v[4:5], v[8:9]
	v_pk_fma_f32 v[2:3], v[6:7], v[6:7], v[2:3]
	s_nop 0
	v_pk_add_f32 v[2:3], v[4:5], v[2:3]
	ds_bpermute_b32 v5, v133, v3
	ds_bpermute_b32 v4, v133, v2
	s_waitcnt lgkmcnt(0)
	v_pk_add_f32 v[2:3], v[2:3], v[4:5]
	ds_bpermute_b32 v5, v134, v3
	ds_bpermute_b32 v4, v134, v2
	s_waitcnt lgkmcnt(0)
	v_pk_add_f32 v[2:3], v[2:3], v[4:5]
	ds_bpermute_b32 v5, v135, v3
	ds_bpermute_b32 v4, v135, v2
	s_waitcnt lgkmcnt(0)
	v_pk_add_f32 v[2:3], v[2:3], v[4:5]
	ds_bpermute_b32 v5, v136, v3
	ds_bpermute_b32 v4, v136, v2
	s_waitcnt lgkmcnt(0)
	v_pk_add_f32 v[2:3], v[2:3], v[4:5]
	ds_bpermute_b32 v5, v137, v3
	ds_bpermute_b32 v4, v137, v2
	s_waitcnt lgkmcnt(0)
	v_pk_add_f32 v[2:3], v[2:3], v[4:5]
	ds_bpermute_b32 v5, v138, v3
	ds_bpermute_b32 v4, v138, v2
	s_waitcnt lgkmcnt(0)
	v_pk_add_f32 v[2:3], v[2:3], v[4:5]
	s_nop 0
	v_pk_fma_f32 v[2:3], v[2:3], s[16:17], v[176:177] op_sel_hi:[1,0,0]
	s_nop 0
	v_mul_f32_e32 v4, 0x4b800000, v3
	v_cmp_gt_f32_e32 vcc, s25, v3
	v_cmp_gt_f32_e64 s[16:17], s25, v2
	s_nop 0
	v_cndmask_b32_e32 v3, v3, v4, vcc
	v_mul_f32_e32 v4, 0x4b800000, v2
	v_rsq_f32_e32 v3, v3
	v_cndmask_b32_e64 v2, v2, v4, s[16:17]
	v_rsq_f32_e32 v2, v2
	v_mul_f32_e32 v4, 0x45800000, v3
	v_cndmask_b32_e32 v4, v3, v4, vcc
	v_mul_f32_e32 v3, 0x45800000, v2
	v_cndmask_b32_e64 v104, v2, v3, s[16:17]
	ds_read_b128 v[76:79], v121
	ds_read_b128 v[86:89], v122
	v_mov_b32_e32 v2, v113
	v_mov_b32_e32 v3, v117
	v_pk_mul_f32 v[2:3], v[2:3], v[4:5] op_sel_hi:[1,0]
	v_mov_b32_e32 v8, v141
	v_mov_b32_e32 v9, v17
	s_waitcnt lgkmcnt(0)
	v_pk_fma_f32 v[94:95], v[76:77], v[2:3], v[86:87]
	v_pk_mul_f32 v[8:9], v[8:9], v[4:5] op_sel_hi:[1,0]
	v_med3_f32 v2, v94, s26, v209
	v_med3_f32 v3, v95, s26, v209
	v_mov_b32_e32 v5, v131
	v_cvt_pk_fp8_f32 v5, v2, v3
	v_pk_fma_f32 v[82:83], v[78:79], v[8:9], v[88:89]
	s_mov_b32 s16, 0x41068000
	v_med3_f32 v2, v82, s26, v209
	v_med3_f32 v3, v83, s26, v209
	v_cvt_pk_fp8_f32 v5, v2, v3 op_sel:[0,0,1]
	v_lshl_add_u64 v[2:3], s[62:63], 0, v[40:41]
	v_add_co_u32_e32 v114, vcc, s16, v2
	v_mov_b32_e32 v113, v116
	s_nop 0
	v_addc_co_u32_e32 v115, vcc, 0, v3, vcc
	v_pk_mul_f32 v[2:3], v[112:113], v[104:105] op_sel_hi:[1,0]
	global_store_dword v[114:115], v5, off
	v_pk_fma_f32 v[96:97], v[76:77], v[2:3], v[86:87]
	v_mov_b32_e32 v5, v131
	v_med3_f32 v2, v96, s26, v209
	v_med3_f32 v3, v97, s26, v209
	v_mov_b32_e32 v141, v16
	v_cvt_pk_fp8_f32 v5, v2, v3
	v_pk_mul_f32 v[8:9], v[140:141], v[104:105] op_sel_hi:[1,0]
	s_nop 0
	v_pk_fma_f32 v[84:85], v[78:79], v[8:9], v[88:89]
	s_nop 0
	v_med3_f32 v2, v84, s26, v209
	v_med3_f32 v3, v85, s26, v209
	v_cvt_pk_fp8_f32 v5, v2, v3 op_sel:[0,0,1]
	v_add_u32_e32 v2, -16, v36
	v_ashrrev_i32_e32 v3, 31, v2
	v_lshlrev_b64 v[8:9], 10, v[2:3]
	v_lshl_add_u64 v[16:17], v[26:27], 0, v[8:9]
	global_store_dword v[16:17], v5, off
	ds_read_b128 v[78:81], v123
	ds_read_b128 v[140:143], v124
	v_mov_b32_e32 v16, v103
	v_mov_b32_e32 v17, v107
	v_pk_mul_f32 v[76:77], v[16:17], v[4:5] op_sel_hi:[1,0]
	v_mov_b32_e32 v16, v109
	v_mov_b32_e32 v17, v111
	s_waitcnt lgkmcnt(0)
	v_pk_fma_f32 v[86:87], v[76:77], v[78:79], v[140:141]
	v_pk_mul_f32 v[16:17], v[16:17], v[4:5] op_sel_hi:[1,0]
	v_med3_f32 v5, v86, s26, v209
	v_med3_f32 v37, v87, s26, v209
	v_mov_b32_e32 v76, v131
	v_cvt_pk_fp8_f32 v76, v5, v37
	v_pk_fma_f32 v[16:17], v[16:17], v[80:81], v[142:143]
	v_mov_b32_e32 v103, v106
	v_med3_f32 v5, v16, s26, v209
	v_med3_f32 v37, v17, s26, v209
	v_cvt_pk_fp8_f32 v76, v5, v37 op_sel:[0,0,1]
	v_pk_mul_f32 v[88:89], v[102:103], v[104:105] op_sel_hi:[1,0]
	v_mov_b32_e32 v109, v110
	v_pk_fma_f32 v[88:89], v[88:89], v[78:79], v[140:141]
	v_mov_b32_e32 v78, v131
	v_med3_f32 v5, v88, s26, v209
	v_med3_f32 v37, v89, s26, v209
	v_cvt_pk_fp8_f32 v78, v5, v37
	global_store_dword v[114:115], v76, off offset:256
	v_pk_mul_f32 v[76:77], v[108:109], v[104:105] op_sel_hi:[1,0]
	v_lshl_add_u64 v[102:103], s[64:65], 0, v[8:9]
	v_pk_fma_f32 v[76:77], v[76:77], v[80:81], v[142:143]
	v_lshl_add_u64 v[8:9], v[102:103], 0, v[28:29]
	v_med3_f32 v5, v76, s26, v209
	v_med3_f32 v37, v77, s26, v209
	v_cvt_pk_fp8_f32 v78, v5, v37 op_sel:[0,0,1]
	v_mov_b32_e32 v37, v131
	global_store_dword v[8:9], v78, off
	ds_read_b128 v[106:109], v125
	ds_read_b128 v[110:113], v126
	v_mov_b32_e32 v8, v11
	v_mov_b32_e32 v9, v13
	v_pk_mul_f32 v[78:79], v[8:9], v[4:5] op_sel_hi:[1,0]
	v_mov_b32_e32 v8, v99
	v_mov_b32_e32 v9, v101
	s_waitcnt lgkmcnt(0)
	v_pk_fma_f32 v[78:79], v[78:79], v[106:107], v[110:111]
	v_pk_mul_f32 v[8:9], v[8:9], v[4:5] op_sel_hi:[1,0]
	v_med3_f32 v5, v78, s26, v209
	v_med3_f32 v11, v79, s26, v209
	v_mov_b32_e32 v13, v131
	v_cvt_pk_fp8_f32 v13, v5, v11
	v_pk_fma_f32 v[8:9], v[8:9], v[108:109], v[112:113]
	v_mov_b32_e32 v99, v100
	v_med3_f32 v5, v8, s26, v209
	v_med3_f32 v11, v9, s26, v209
	v_cvt_pk_fp8_f32 v13, v5, v11 op_sel:[0,0,1]
	v_mov_b32_e32 v11, v12
	v_pk_mul_f32 v[10:11], v[10:11], v[104:105] op_sel_hi:[1,0]
	global_store_dword v[114:115], v13, off offset:512
	v_pk_fma_f32 v[80:81], v[10:11], v[106:107], v[110:111]
	v_pk_mul_f32 v[12:13], v[98:99], v[104:105] op_sel_hi:[1,0]
	v_med3_f32 v5, v80, s26, v209
	v_med3_f32 v10, v81, s26, v209
	v_cvt_pk_fp8_f32 v37, v5, v10
	v_pk_fma_f32 v[12:13], v[12:13], v[108:109], v[112:113]
	v_mov_b32_e32 v111, v7
	v_med3_f32 v5, v12, s26, v209
	v_med3_f32 v10, v13, s26, v209
	v_cvt_pk_fp8_f32 v37, v5, v10 op_sel:[0,0,1]
	v_lshl_add_u64 v[10:11], v[102:103], 0, v[30:31]
	v_mov_b32_e32 v110, v93
	v_mov_b32_e32 v93, v6
	global_store_dword v[10:11], v37, off
	ds_read_b128 v[98:101], v127
	ds_read_b128 v[106:109], v128
	v_mov_b32_e32 v10, v15
	v_mov_b32_e32 v11, v91
	v_pk_mul_f32 v[10:11], v[10:11], v[4:5] op_sel_hi:[1,0]
	v_mov_b32_e32 v37, v131
	s_waitcnt lgkmcnt(0)
	v_pk_fma_f32 v[10:11], v[10:11], v[98:99], v[106:107]
	v_pk_mul_f32 v[4:5], v[110:111], v[4:5] op_sel_hi:[1,0]
	v_med3_f32 v7, v10, s26, v209
	v_med3_f32 v15, v11, s26, v209
	v_cvt_pk_fp8_f32 v37, v7, v15
	v_pk_fma_f32 v[4:5], v[4:5], v[100:101], v[108:109]
	s_nop 0
	v_med3_f32 v7, v4, s26, v209
	v_med3_f32 v15, v5, s26, v209
	v_cvt_pk_fp8_f32 v37, v7, v15 op_sel:[0,0,1]
	v_mov_b32_e32 v15, v90
	v_pk_mul_f32 v[14:15], v[14:15], v[104:105] op_sel_hi:[1,0]
	v_pk_mul_f32 v[6:7], v[92:93], v[104:105] op_sel_hi:[1,0]
	v_pk_fma_f32 v[14:15], v[14:15], v[98:99], v[106:107]
	global_store_dword v[114:115], v37, off offset:768
	v_med3_f32 v37, v14, s26, v209
	v_med3_f32 v90, v15, s26, v209
	v_mov_b32_e32 v92, v131
	v_cvt_pk_fp8_f32 v92, v37, v90
	v_pk_fma_f32 v[6:7], v[6:7], v[100:101], v[108:109]
	s_nop 0
	v_med3_f32 v37, v6, s26, v209
	v_med3_f32 v90, v7, s26, v209
	v_cvt_pk_fp8_f32 v92, v37, v90 op_sel:[0,0,1]
	v_lshl_add_u64 v[90:91], v[102:103], 0, v[32:33]
	global_store_dword v[90:91], v92, off
	v_mov_b32_e32 v37, v120
	v_mov_b32_e32 v110, v94
	v_add_u32_e32 v37, 0, v37
	ds_read_b128 v[90:93], v37
	ds_read_b128 v[98:101], v37 offset:16
	ds_read_b128 v[102:105], v37 offset:32
	ds_read_b128 v[106:109], v37 offset:48
	v_mov_b32_e32 v111, v96
	s_waitcnt lgkmcnt(3)
	v_pk_fma_f32 v[112:113], v[110:111], v[90:91], 0 op_sel_hi:[1,0,0]
	v_pk_fma_f32 v[114:115], v[110:111], v[90:91], 0 op_sel:[0,1,0] op_sel_hi:[1,1,0]
	v_mov_b32_e32 v90, v93
	v_pk_fma_f32 v[140:141], v[110:111], v[90:91], 0 op_sel_hi:[1,0,0]
	s_waitcnt lgkmcnt(2)
	v_mov_b32_e32 v90, v101
	v_pk_fma_f32 v[148:149], v[110:111], v[90:91], 0 op_sel_hi:[1,0,0]
	s_waitcnt lgkmcnt(1)
	v_mov_b32_e32 v90, v105
	v_pk_fma_f32 v[156:157], v[110:111], v[90:91], 0 op_sel_hi:[1,0,0]
	s_waitcnt lgkmcnt(0)
	v_mov_b32_e32 v90, v109
	v_pk_fma_f32 v[116:117], v[110:111], v[92:93], 0 op_sel_hi:[1,0,0]
	v_pk_fma_f32 v[142:143], v[110:111], v[98:99], 0 op_sel_hi:[1,0,0]
	v_pk_fma_f32 v[144:145], v[110:111], v[98:99], 0 op_sel:[0,1,0] op_sel_hi:[1,1,0]
	v_pk_fma_f32 v[146:147], v[110:111], v[100:101], 0 op_sel_hi:[1,0,0]
	v_pk_fma_f32 v[150:151], v[110:111], v[102:103], 0 op_sel_hi:[1,0,0]
	v_pk_fma_f32 v[152:153], v[110:111], v[102:103], 0 op_sel:[0,1,0] op_sel_hi:[1,1,0]
	v_pk_fma_f32 v[154:155], v[110:111], v[104:105], 0 op_sel_hi:[1,0,0]
	v_pk_fma_f32 v[158:159], v[110:111], v[106:107], 0 op_sel_hi:[1,0,0]
	v_pk_fma_f32 v[160:161], v[110:111], v[106:107], 0 op_sel:[0,1,0] op_sel_hi:[1,1,0]
	v_pk_fma_f32 v[162:163], v[110:111], v[108:109], 0 op_sel_hi:[1,0,0]
	v_pk_fma_f32 v[110:111], v[110:111], v[90:91], 0 op_sel_hi:[1,0,0]
	ds_read_b128 v[90:93], v37 offset:20480
	ds_read_b128 v[98:101], v37 offset:20496
	ds_read_b128 v[102:105], v37 offset:20512
	ds_read_b128 v[106:109], v37 offset:20528
	v_mov_b32_e32 v96, v95
	s_waitcnt lgkmcnt(3)
	v_pk_fma_f32 v[112:113], v[96:97], v[90:91], v[112:113] op_sel_hi:[1,0,1]
	v_pk_fma_f32 v[114:115], v[96:97], v[90:91], v[114:115] op_sel:[0,1,0]
	v_mov_b32_e32 v90, v93
	v_pk_fma_f32 v[140:141], v[96:97], v[90:91], v[140:141] op_sel_hi:[1,0,1]
	s_waitcnt lgkmcnt(2)
	v_mov_b32_e32 v90, v101
	v_pk_fma_f32 v[148:149], v[96:97], v[90:91], v[148:149] op_sel_hi:[1,0,1]
	s_waitcnt lgkmcnt(1)
	v_mov_b32_e32 v90, v105
	v_pk_fma_f32 v[156:157], v[96:97], v[90:91], v[156:157] op_sel_hi:[1,0,1]
	s_waitcnt lgkmcnt(0)
	v_mov_b32_e32 v90, v109
	v_pk_fma_f32 v[116:117], v[96:97], v[92:93], v[116:117] op_sel_hi:[1,0,1]
	v_pk_fma_f32 v[142:143], v[96:97], v[98:99], v[142:143] op_sel_hi:[1,0,1]
	v_pk_fma_f32 v[144:145], v[96:97], v[98:99], v[144:145] op_sel:[0,1,0]
	v_pk_fma_f32 v[146:147], v[96:97], v[100:101], v[146:147] op_sel_hi:[1,0,1]
	v_pk_fma_f32 v[150:151], v[96:97], v[102:103], v[150:151] op_sel_hi:[1,0,1]
	v_pk_fma_f32 v[152:153], v[96:97], v[102:103], v[152:153] op_sel:[0,1,0]
	v_pk_fma_f32 v[154:155], v[96:97], v[104:105], v[154:155] op_sel_hi:[1,0,1]
	v_pk_fma_f32 v[158:159], v[96:97], v[106:107], v[158:159] op_sel_hi:[1,0,1]
	v_pk_fma_f32 v[106:107], v[96:97], v[106:107], v[160:161] op_sel:[0,1,0]
	v_pk_fma_f32 v[160:161], v[96:97], v[108:109], v[162:163] op_sel_hi:[1,0,1]
	v_pk_fma_f32 v[108:109], v[96:97], v[90:91], v[110:111] op_sel_hi:[1,0,1]
	ds_read_b128 v[90:93], v37 offset:40960
	ds_read_b128 v[94:97], v37 offset:40976
	ds_read_b128 v[98:101], v37 offset:40992
	ds_read_b128 v[102:105], v37 offset:41008
	v_mov_b32_e32 v110, v82
	v_mov_b32_e32 v111, v84
	s_waitcnt lgkmcnt(3)
	v_mov_b32_e32 v82, v93
	v_pk_fma_f32 v[140:141], v[110:111], v[82:83], v[140:141] op_sel_hi:[1,0,1]
	s_waitcnt lgkmcnt(2)
	v_mov_b32_e32 v82, v97
	v_pk_fma_f32 v[148:149], v[110:111], v[82:83], v[148:149] op_sel_hi:[1,0,1]
	s_waitcnt lgkmcnt(1)
	v_mov_b32_e32 v82, v101
	v_pk_fma_f32 v[156:157], v[110:111], v[82:83], v[156:157] op_sel_hi:[1,0,1]
	s_waitcnt lgkmcnt(0)
	v_mov_b32_e32 v82, v105
	v_pk_fma_f32 v[112:113], v[110:111], v[90:91], v[112:113] op_sel_hi:[1,0,1]
	v_pk_fma_f32 v[114:115], v[110:111], v[90:91], v[114:115] op_sel:[0,1,0]
	v_pk_fma_f32 v[116:117], v[110:111], v[92:93], v[116:117] op_sel_hi:[1,0,1]
	v_pk_fma_f32 v[142:143], v[110:111], v[94:95], v[142:143] op_sel_hi:[1,0,1]
	v_pk_fma_f32 v[144:145], v[110:111], v[94:95], v[144:145] op_sel:[0,1,0]
	v_pk_fma_f32 v[146:147], v[110:111], v[96:97], v[146:147] op_sel_hi:[1,0,1]
	v_pk_fma_f32 v[150:151], v[110:111], v[98:99], v[150:151] op_sel_hi:[1,0,1]
	v_pk_fma_f32 v[152:153], v[110:111], v[98:99], v[152:153] op_sel:[0,1,0]
	v_pk_fma_f32 v[154:155], v[110:111], v[100:101], v[154:155] op_sel_hi:[1,0,1]
	v_pk_fma_f32 v[158:159], v[110:111], v[102:103], v[158:159] op_sel_hi:[1,0,1]
	v_pk_fma_f32 v[106:107], v[110:111], v[102:103], v[106:107] op_sel:[0,1,0]
	v_pk_fma_f32 v[160:161], v[110:111], v[104:105], v[160:161] op_sel_hi:[1,0,1]
	v_pk_fma_f32 v[108:109], v[110:111], v[82:83], v[108:109] op_sel_hi:[1,0,1]
	ds_read_b128 v[90:93], v37 offset:61440
	ds_read_b128 v[94:97], v37 offset:61456
	ds_read_b128 v[98:101], v37 offset:61472
	ds_read_b128 v[102:105], v37 offset:61488
	v_mov_b32_e32 v84, v83
	s_waitcnt lgkmcnt(3)
	v_mov_b32_e32 v82, v93
	v_pk_fma_f32 v[110:111], v[84:85], v[90:91], v[112:113] op_sel_hi:[1,0,1]
	v_pk_fma_f32 v[112:113], v[84:85], v[90:91], v[114:115] op_sel:[0,1,0]
	v_pk_fma_f32 v[114:115], v[84:85], v[92:93], v[116:117] op_sel_hi:[1,0,1]
	v_pk_fma_f32 v[116:117], v[84:85], v[82:83], v[140:141] op_sel_hi:[1,0,1]
	s_waitcnt lgkmcnt(2)
	v_mov_b32_e32 v82, v97
	v_pk_fma_f32 v[140:141], v[84:85], v[94:95], v[142:143] op_sel_hi:[1,0,1]
	v_pk_fma_f32 v[142:143], v[84:85], v[94:95], v[144:145] op_sel:[0,1,0]
	v_pk_fma_f32 v[144:145], v[84:85], v[96:97], v[146:147] op_sel_hi:[1,0,1]
	v_pk_fma_f32 v[146:147], v[84:85], v[82:83], v[148:149] op_sel_hi:[1,0,1]
	s_waitcnt lgkmcnt(1)
	v_mov_b32_e32 v82, v101
	v_pk_fma_f32 v[148:149], v[84:85], v[98:99], v[150:151] op_sel_hi:[1,0,1]
	v_pk_fma_f32 v[150:151], v[84:85], v[98:99], v[152:153] op_sel:[0,1,0]
	v_pk_fma_f32 v[152:153], v[84:85], v[100:101], v[154:155] op_sel_hi:[1,0,1]
	v_pk_fma_f32 v[154:155], v[84:85], v[82:83], v[156:157] op_sel_hi:[1,0,1]
	s_waitcnt lgkmcnt(0)
	v_mov_b32_e32 v82, v105
	v_pk_fma_f32 v[156:157], v[84:85], v[102:103], v[158:159] op_sel_hi:[1,0,1]
	v_pk_fma_f32 v[102:103], v[84:85], v[102:103], v[106:107] op_sel:[0,1,0]
	v_pk_fma_f32 v[106:107], v[84:85], v[104:105], v[160:161] op_sel_hi:[1,0,1]
	v_pk_fma_f32 v[104:105], v[84:85], v[82:83], v[108:109] op_sel_hi:[1,0,1]
	ds_read_b128 v[82:85], v37 offset:5120
	ds_read_b128 v[90:93], v37 offset:5136
	ds_read_b128 v[94:97], v37 offset:5152
	ds_read_b128 v[98:101], v37 offset:5168
	v_mov_b32_e32 v108, v86
	v_mov_b32_e32 v109, v88
	s_waitcnt lgkmcnt(3)
	v_pk_fma_f32 v[110:111], v[108:109], v[82:83], v[110:111] op_sel_hi:[1,0,1]
	v_pk_fma_f32 v[112:113], v[108:109], v[82:83], v[112:113] op_sel:[0,1,0]
	v_mov_b32_e32 v82, v85
	v_pk_fma_f32 v[116:117], v[108:109], v[82:83], v[116:117] op_sel_hi:[1,0,1]
	s_waitcnt lgkmcnt(2)
	v_mov_b32_e32 v82, v93
	v_pk_fma_f32 v[146:147], v[108:109], v[82:83], v[146:147] op_sel_hi:[1,0,1]
	s_waitcnt lgkmcnt(1)
	v_mov_b32_e32 v82, v97
	v_pk_fma_f32 v[154:155], v[108:109], v[82:83], v[154:155] op_sel_hi:[1,0,1]
	s_waitcnt lgkmcnt(0)
	v_mov_b32_e32 v82, v101
	v_pk_fma_f32 v[114:115], v[108:109], v[84:85], v[114:115] op_sel_hi:[1,0,1]
	v_pk_fma_f32 v[140:141], v[108:109], v[90:91], v[140:141] op_sel_hi:[1,0,1]
	v_pk_fma_f32 v[142:143], v[108:109], v[90:91], v[142:143] op_sel:[0,1,0]
	v_pk_fma_f32 v[144:145], v[108:109], v[92:93], v[144:145] op_sel_hi:[1,0,1]
	v_pk_fma_f32 v[148:149], v[108:109], v[94:95], v[148:149] op_sel_hi:[1,0,1]
	v_pk_fma_f32 v[150:151], v[108:109], v[94:95], v[150:151] op_sel:[0,1,0]
	v_pk_fma_f32 v[152:153], v[108:109], v[96:97], v[152:153] op_sel_hi:[1,0,1]
	v_pk_fma_f32 v[156:157], v[108:109], v[98:99], v[156:157] op_sel_hi:[1,0,1]
	v_pk_fma_f32 v[102:103], v[108:109], v[98:99], v[102:103] op_sel:[0,1,0]
	v_pk_fma_f32 v[106:107], v[108:109], v[100:101], v[106:107] op_sel_hi:[1,0,1]
	v_pk_fma_f32 v[104:105], v[108:109], v[82:83], v[104:105] op_sel_hi:[1,0,1]
	ds_read_b128 v[82:85], v37 offset:25600
	ds_read_b128 v[90:93], v37 offset:25616
	ds_read_b128 v[94:97], v37 offset:25632
	ds_read_b128 v[98:101], v37 offset:25648
	v_mov_b32_e32 v88, v87
	s_waitcnt lgkmcnt(3)
	v_pk_fma_f32 v[108:109], v[88:89], v[82:83], v[110:111] op_sel_hi:[1,0,1]
	v_pk_fma_f32 v[110:111], v[88:89], v[82:83], v[112:113] op_sel:[0,1,0]
	v_mov_b32_e32 v82, v85
	v_pk_fma_f32 v[112:113], v[88:89], v[84:85], v[114:115] op_sel_hi:[1,0,1]
	v_pk_fma_f32 v[114:115], v[88:89], v[82:83], v[116:117] op_sel_hi:[1,0,1]
	s_waitcnt lgkmcnt(2)
	v_mov_b32_e32 v82, v93
	v_pk_fma_f32 v[116:117], v[88:89], v[90:91], v[140:141] op_sel_hi:[1,0,1]
	v_pk_fma_f32 v[140:141], v[88:89], v[90:91], v[142:143] op_sel:[0,1,0]
	v_pk_fma_f32 v[142:143], v[88:89], v[92:93], v[144:145] op_sel_hi:[1,0,1]
	v_pk_fma_f32 v[144:145], v[88:89], v[82:83], v[146:147] op_sel_hi:[1,0,1]
	s_waitcnt lgkmcnt(1)
	v_mov_b32_e32 v82, v97
	v_pk_fma_f32 v[146:147], v[88:89], v[94:95], v[148:149] op_sel_hi:[1,0,1]
	v_pk_fma_f32 v[148:149], v[88:89], v[94:95], v[150:151] op_sel:[0,1,0]
	v_pk_fma_f32 v[150:151], v[88:89], v[96:97], v[152:153] op_sel_hi:[1,0,1]
	v_pk_fma_f32 v[152:153], v[88:89], v[82:83], v[154:155] op_sel_hi:[1,0,1]
	s_waitcnt lgkmcnt(0)
	v_mov_b32_e32 v82, v101
	v_pk_fma_f32 v[154:155], v[88:89], v[98:99], v[156:157] op_sel_hi:[1,0,1]
	v_pk_fma_f32 v[98:99], v[88:89], v[98:99], v[102:103] op_sel:[0,1,0]
	v_pk_fma_f32 v[102:103], v[88:89], v[100:101], v[106:107] op_sel_hi:[1,0,1]
	v_pk_fma_f32 v[100:101], v[88:89], v[82:83], v[104:105] op_sel_hi:[1,0,1]
	ds_read_b128 v[82:85], v37 offset:46080
	ds_read_b128 v[86:89], v37 offset:46096
	ds_read_b128 v[90:93], v37 offset:46112
	ds_read_b128 v[94:97], v37 offset:46128
	v_mov_b32_e32 v104, v16
	v_mov_b32_e32 v105, v76
	s_waitcnt lgkmcnt(3)
	v_mov_b32_e32 v16, v85
	v_pk_fma_f32 v[106:107], v[104:105], v[82:83], v[108:109] op_sel_hi:[1,0,1]
	v_pk_fma_f32 v[108:109], v[104:105], v[82:83], v[110:111] op_sel:[0,1,0]
	v_pk_fma_f32 v[110:111], v[104:105], v[84:85], v[112:113] op_sel_hi:[1,0,1]
	v_pk_fma_f32 v[112:113], v[104:105], v[16:17], v[114:115] op_sel_hi:[1,0,1]
	s_waitcnt lgkmcnt(2)
	v_mov_b32_e32 v16, v89
	v_pk_fma_f32 v[114:115], v[104:105], v[86:87], v[116:117] op_sel_hi:[1,0,1]
	v_pk_fma_f32 v[116:117], v[104:105], v[86:87], v[140:141] op_sel:[0,1,0]
	v_pk_fma_f32 v[140:141], v[104:105], v[88:89], v[142:143] op_sel_hi:[1,0,1]
	v_pk_fma_f32 v[142:143], v[104:105], v[16:17], v[144:145] op_sel_hi:[1,0,1]
	s_waitcnt lgkmcnt(1)
	v_mov_b32_e32 v16, v93
	v_pk_fma_f32 v[144:145], v[104:105], v[90:91], v[146:147] op_sel_hi:[1,0,1]
	v_pk_fma_f32 v[146:147], v[104:105], v[90:91], v[148:149] op_sel:[0,1,0]
	v_pk_fma_f32 v[148:149], v[104:105], v[92:93], v[150:151] op_sel_hi:[1,0,1]
	v_pk_fma_f32 v[150:151], v[104:105], v[16:17], v[152:153] op_sel_hi:[1,0,1]
	s_waitcnt lgkmcnt(0)
	v_mov_b32_e32 v16, v97
	v_pk_fma_f32 v[152:153], v[104:105], v[94:95], v[154:155] op_sel_hi:[1,0,1]
	v_pk_fma_f32 v[98:99], v[104:105], v[94:95], v[98:99] op_sel:[0,1,0]
	v_pk_fma_f32 v[102:103], v[104:105], v[96:97], v[102:103] op_sel_hi:[1,0,1]
	v_pk_fma_f32 v[100:101], v[104:105], v[16:17], v[100:101] op_sel_hi:[1,0,1]
	v_add_u32_e32 v16, 0x10400, v37
	v_add_u32_e32 v76, 0x10410, v37
	ds_read_b128 v[82:85], v16
	ds_read_b128 v[86:89], v76
	v_add_u32_e32 v16, 0x10420, v37
	v_add_u32_e32 v76, 0x10430, v37
	ds_read_b128 v[90:93], v16
	ds_read_b128 v[94:97], v76
	v_mov_b32_e32 v76, v17
	s_waitcnt lgkmcnt(3)
	v_pk_fma_f32 v[16:17], v[76:77], v[82:83], v[106:107] op_sel_hi:[1,0,1]
	v_pk_fma_f32 v[104:105], v[76:77], v[82:83], v[108:109] op_sel:[0,1,0]
	v_mov_b32_e32 v82, v85
	v_pk_fma_f32 v[108:109], v[76:77], v[82:83], v[112:113] op_sel_hi:[1,0,1]
	s_waitcnt lgkmcnt(2)
	v_mov_b32_e32 v82, v89
	v_pk_fma_f32 v[112:113], v[76:77], v[86:87], v[116:117] op_sel:[0,1,0]
	v_pk_fma_f32 v[116:117], v[76:77], v[82:83], v[142:143] op_sel_hi:[1,0,1]
	s_waitcnt lgkmcnt(1)
	v_mov_b32_e32 v82, v93
	v_pk_fma_f32 v[142:143], v[76:77], v[90:91], v[146:147] op_sel:[0,1,0]
	v_pk_fma_f32 v[146:147], v[76:77], v[82:83], v[150:151] op_sel_hi:[1,0,1]
	s_waitcnt lgkmcnt(0)
	v_mov_b32_e32 v82, v97
	v_pk_fma_f32 v[106:107], v[76:77], v[84:85], v[110:111] op_sel_hi:[1,0,1]
	v_pk_fma_f32 v[110:111], v[76:77], v[86:87], v[114:115] op_sel_hi:[1,0,1]
	v_pk_fma_f32 v[114:115], v[76:77], v[88:89], v[140:141] op_sel_hi:[1,0,1]
	v_pk_fma_f32 v[140:141], v[76:77], v[90:91], v[144:145] op_sel_hi:[1,0,1]
	v_pk_fma_f32 v[144:145], v[76:77], v[92:93], v[148:149] op_sel_hi:[1,0,1]
	v_pk_fma_f32 v[148:149], v[76:77], v[94:95], v[152:153] op_sel_hi:[1,0,1]
	v_pk_fma_f32 v[98:99], v[76:77], v[94:95], v[98:99] op_sel:[0,1,0]
	v_pk_fma_f32 v[102:103], v[76:77], v[96:97], v[102:103] op_sel_hi:[1,0,1]
	v_pk_fma_f32 v[76:77], v[76:77], v[82:83], v[100:101] op_sel_hi:[1,0,1]
	ds_read_b128 v[82:85], v37 offset:10240
	ds_read_b128 v[86:89], v37 offset:10256
	ds_read_b128 v[90:93], v37 offset:10272
	ds_read_b128 v[94:97], v37 offset:10288
	v_mov_b32_e32 v100, v78
	v_mov_b32_e32 v101, v80
	s_waitcnt lgkmcnt(3)
	v_mov_b32_e32 v78, v85
	v_pk_fma_f32 v[108:109], v[100:101], v[78:79], v[108:109] op_sel_hi:[1,0,1]
	s_waitcnt lgkmcnt(2)
	v_mov_b32_e32 v78, v89
	v_pk_fma_f32 v[116:117], v[100:101], v[78:79], v[116:117] op_sel_hi:[1,0,1]
	s_waitcnt lgkmcnt(1)
	v_mov_b32_e32 v78, v93
	v_pk_fma_f32 v[146:147], v[100:101], v[78:79], v[146:147] op_sel_hi:[1,0,1]
	s_waitcnt lgkmcnt(0)
	v_mov_b32_e32 v78, v97
	v_pk_fma_f32 v[16:17], v[100:101], v[82:83], v[16:17] op_sel_hi:[1,0,1]
	v_pk_fma_f32 v[76:77], v[100:101], v[78:79], v[76:77] op_sel_hi:[1,0,1]
	v_pk_fma_f32 v[104:105], v[100:101], v[82:83], v[104:105] op_sel:[0,1,0]
	v_pk_fma_f32 v[106:107], v[100:101], v[84:85], v[106:107] op_sel_hi:[1,0,1]
	v_pk_fma_f32 v[110:111], v[100:101], v[86:87], v[110:111] op_sel_hi:[1,0,1]
	v_pk_fma_f32 v[112:113], v[100:101], v[86:87], v[112:113] op_sel:[0,1,0]
	v_pk_fma_f32 v[114:115], v[100:101], v[88:89], v[114:115] op_sel_hi:[1,0,1]
	v_pk_fma_f32 v[140:141], v[100:101], v[90:91], v[140:141] op_sel_hi:[1,0,1]
	v_pk_fma_f32 v[142:143], v[100:101], v[90:91], v[142:143] op_sel:[0,1,0]
	v_pk_fma_f32 v[144:145], v[100:101], v[92:93], v[144:145] op_sel_hi:[1,0,1]
	v_pk_fma_f32 v[148:149], v[100:101], v[94:95], v[148:149] op_sel_hi:[1,0,1]
	v_pk_fma_f32 v[98:99], v[100:101], v[94:95], v[98:99] op_sel:[0,1,0]
	v_pk_fma_f32 v[102:103], v[100:101], v[96:97], v[102:103] op_sel_hi:[1,0,1]
	ds_read_b128 v[82:85], v37 offset:30720
	ds_read_b128 v[86:89], v37 offset:30736
	ds_read_b128 v[90:93], v37 offset:30752
	ds_read_b128 v[94:97], v37 offset:30768
	v_mov_b32_e32 v80, v79
	s_waitcnt lgkmcnt(3)
	v_mov_b32_e32 v78, v85
	v_pk_fma_f32 v[100:101], v[80:81], v[82:83], v[104:105] op_sel:[0,1,0]
	v_pk_fma_f32 v[104:105], v[80:81], v[84:85], v[106:107] op_sel_hi:[1,0,1]
	v_pk_fma_f32 v[106:107], v[80:81], v[78:79], v[108:109] op_sel_hi:[1,0,1]
	s_waitcnt lgkmcnt(2)
	v_mov_b32_e32 v78, v89
	v_pk_fma_f32 v[108:109], v[80:81], v[86:87], v[110:111] op_sel_hi:[1,0,1]
	v_pk_fma_f32 v[110:111], v[80:81], v[86:87], v[112:113] op_sel:[0,1,0]
	v_pk_fma_f32 v[112:113], v[80:81], v[88:89], v[114:115] op_sel_hi:[1,0,1]
	v_pk_fma_f32 v[114:115], v[80:81], v[78:79], v[116:117] op_sel_hi:[1,0,1]
	s_waitcnt lgkmcnt(1)
	v_mov_b32_e32 v78, v93
	v_pk_fma_f32 v[16:17], v[80:81], v[82:83], v[16:17] op_sel_hi:[1,0,1]
	v_pk_fma_f32 v[116:117], v[80:81], v[90:91], v[140:141] op_sel_hi:[1,0,1]
	v_pk_fma_f32 v[140:141], v[80:81], v[90:91], v[142:143] op_sel:[0,1,0]
	v_pk_fma_f32 v[142:143], v[80:81], v[92:93], v[144:145] op_sel_hi:[1,0,1]
	v_pk_fma_f32 v[92:93], v[80:81], v[78:79], v[146:147] op_sel_hi:[1,0,1]
	s_waitcnt lgkmcnt(0)
	v_mov_b32_e32 v78, v97
	v_pk_fma_f32 v[144:145], v[80:81], v[94:95], v[148:149] op_sel_hi:[1,0,1]
	v_pk_fma_f32 v[94:95], v[80:81], v[94:95], v[98:99] op_sel:[0,1,0]
	v_pk_fma_f32 v[98:99], v[80:81], v[96:97], v[102:103] op_sel_hi:[1,0,1]
	v_pk_fma_f32 v[96:97], v[80:81], v[78:79], v[76:77] op_sel_hi:[1,0,1]
	ds_read_b128 v[76:79], v37 offset:51200
	ds_read_b128 v[80:83], v37 offset:51216
	ds_read_b128 v[84:87], v37 offset:51232
	ds_read_b128 v[88:91], v37 offset:51248
	v_mov_b32_e32 v102, v8
	v_mov_b32_e32 v103, v12
	s_waitcnt lgkmcnt(3)
	v_mov_b32_e32 v8, v79
	v_pk_fma_f32 v[106:107], v[102:103], v[8:9], v[106:107] op_sel_hi:[1,0,1]
	s_waitcnt lgkmcnt(2)
	v_mov_b32_e32 v8, v83
	v_pk_fma_f32 v[114:115], v[102:103], v[8:9], v[114:115] op_sel_hi:[1,0,1]
	s_waitcnt lgkmcnt(1)
	v_mov_b32_e32 v8, v87
	v_pk_fma_f32 v[16:17], v[102:103], v[76:77], v[16:17] op_sel_hi:[1,0,1]
	v_pk_fma_f32 v[92:93], v[102:103], v[8:9], v[92:93] op_sel_hi:[1,0,1]
	s_waitcnt lgkmcnt(0)
	v_mov_b32_e32 v8, v91
	v_pk_fma_f32 v[100:101], v[102:103], v[76:77], v[100:101] op_sel:[0,1,0]
	v_pk_fma_f32 v[104:105], v[102:103], v[78:79], v[104:105] op_sel_hi:[1,0,1]
	v_pk_fma_f32 v[108:109], v[102:103], v[80:81], v[108:109] op_sel_hi:[1,0,1]
	v_pk_fma_f32 v[110:111], v[102:103], v[80:81], v[110:111] op_sel:[0,1,0]
	v_pk_fma_f32 v[112:113], v[102:103], v[82:83], v[112:113] op_sel_hi:[1,0,1]
	v_pk_fma_f32 v[116:117], v[102:103], v[84:85], v[116:117] op_sel_hi:[1,0,1]
	v_pk_fma_f32 v[140:141], v[102:103], v[84:85], v[140:141] op_sel:[0,1,0]
	v_pk_fma_f32 v[142:143], v[102:103], v[86:87], v[142:143] op_sel_hi:[1,0,1]
	v_pk_fma_f32 v[144:145], v[102:103], v[88:89], v[144:145] op_sel_hi:[1,0,1]
	v_pk_fma_f32 v[94:95], v[102:103], v[88:89], v[94:95] op_sel:[0,1,0]
	v_pk_fma_f32 v[98:99], v[102:103], v[90:91], v[98:99] op_sel_hi:[1,0,1]
	v_pk_fma_f32 v[96:97], v[102:103], v[8:9], v[96:97] op_sel_hi:[1,0,1]
	v_add_u32_e32 v8, 0x11800, v37
	v_add_u32_e32 v12, 0x11810, v37
	ds_read_b128 v[76:79], v8
	ds_read_b128 v[80:83], v12
	v_add_u32_e32 v8, 0x11820, v37
	v_add_u32_e32 v12, 0x11830, v37
	ds_read_b128 v[84:87], v8
	ds_read_b128 v[88:91], v12
	v_mov_b32_e32 v12, v9
	s_waitcnt lgkmcnt(3)
	v_pk_fma_f32 v[8:9], v[12:13], v[76:77], v[16:17] op_sel_hi:[1,0,1]
	v_pk_fma_f32 v[16:17], v[12:13], v[76:77], v[100:101] op_sel:[0,1,0]
	v_mov_b32_e32 v76, v79
	v_pk_fma_f32 v[102:103], v[12:13], v[76:77], v[106:107] op_sel_hi:[1,0,1]
	s_waitcnt lgkmcnt(2)
	v_mov_b32_e32 v76, v83
	v_pk_fma_f32 v[106:107], v[12:13], v[80:81], v[110:111] op_sel:[0,1,0]
	v_pk_fma_f32 v[110:111], v[12:13], v[76:77], v[114:115] op_sel_hi:[1,0,1]
	s_waitcnt lgkmcnt(1)
	v_mov_b32_e32 v76, v87
	v_pk_fma_f32 v[92:93], v[12:13], v[76:77], v[92:93] op_sel_hi:[1,0,1]
	s_waitcnt lgkmcnt(0)
	v_mov_b32_e32 v76, v91
	v_pk_fma_f32 v[100:101], v[12:13], v[78:79], v[104:105] op_sel_hi:[1,0,1]
	v_pk_fma_f32 v[104:105], v[12:13], v[80:81], v[108:109] op_sel_hi:[1,0,1]
	v_pk_fma_f32 v[108:109], v[12:13], v[82:83], v[112:113] op_sel_hi:[1,0,1]
	v_pk_fma_f32 v[112:113], v[12:13], v[84:85], v[116:117] op_sel_hi:[1,0,1]
	v_pk_fma_f32 v[114:115], v[12:13], v[84:85], v[140:141] op_sel:[0,1,0]
	v_pk_fma_f32 v[116:117], v[12:13], v[86:87], v[142:143] op_sel_hi:[1,0,1]
	v_pk_fma_f32 v[140:141], v[12:13], v[88:89], v[144:145] op_sel_hi:[1,0,1]
	v_pk_fma_f32 v[94:95], v[12:13], v[88:89], v[94:95] op_sel:[0,1,0]
	v_pk_fma_f32 v[98:99], v[12:13], v[90:91], v[98:99] op_sel_hi:[1,0,1]
	v_pk_fma_f32 v[12:13], v[12:13], v[76:77], v[96:97] op_sel_hi:[1,0,1]
	ds_read_b128 v[76:79], v37 offset:15360
	ds_read_b128 v[80:83], v37 offset:15376
	ds_read_b128 v[84:87], v37 offset:15392
	ds_read_b128 v[88:91], v37 offset:15408
	v_mov_b32_e32 v96, v10
	v_mov_b32_e32 v97, v14
	s_waitcnt lgkmcnt(3)
	v_mov_b32_e32 v10, v79
	v_pk_fma_f32 v[102:103], v[96:97], v[10:11], v[102:103] op_sel_hi:[1,0,1]
	s_waitcnt lgkmcnt(2)
	v_mov_b32_e32 v10, v83
	v_pk_fma_f32 v[110:111], v[96:97], v[10:11], v[110:111] op_sel_hi:[1,0,1]
	s_waitcnt lgkmcnt(1)
	v_mov_b32_e32 v10, v87
	v_pk_fma_f32 v[92:93], v[96:97], v[10:11], v[92:93] op_sel_hi:[1,0,1]
	s_waitcnt lgkmcnt(0)
	v_mov_b32_e32 v10, v91
	v_pk_fma_f32 v[8:9], v[96:97], v[76:77], v[8:9] op_sel_hi:[1,0,1]
	v_pk_fma_f32 v[16:17], v[96:97], v[76:77], v[16:17] op_sel:[0,1,0]
	v_pk_fma_f32 v[12:13], v[96:97], v[10:11], v[12:13] op_sel_hi:[1,0,1]
	v_pk_fma_f32 v[100:101], v[96:97], v[78:79], v[100:101] op_sel_hi:[1,0,1]
	v_pk_fma_f32 v[104:105], v[96:97], v[80:81], v[104:105] op_sel_hi:[1,0,1]
	v_pk_fma_f32 v[106:107], v[96:97], v[80:81], v[106:107] op_sel:[0,1,0]
	v_pk_fma_f32 v[108:109], v[96:97], v[82:83], v[108:109] op_sel_hi:[1,0,1]
	v_pk_fma_f32 v[112:113], v[96:97], v[84:85], v[112:113] op_sel_hi:[1,0,1]
	v_pk_fma_f32 v[114:115], v[96:97], v[84:85], v[114:115] op_sel:[0,1,0]
	v_pk_fma_f32 v[116:117], v[96:97], v[86:87], v[116:117] op_sel_hi:[1,0,1]
	v_pk_fma_f32 v[140:141], v[96:97], v[88:89], v[140:141] op_sel_hi:[1,0,1]
	v_pk_fma_f32 v[94:95], v[96:97], v[88:89], v[94:95] op_sel:[0,1,0]
	v_pk_fma_f32 v[98:99], v[96:97], v[90:91], v[98:99] op_sel_hi:[1,0,1]
	ds_read_b128 v[76:79], v37 offset:35840
	ds_read_b128 v[80:83], v37 offset:35856
	ds_read_b128 v[84:87], v37 offset:35872
	ds_read_b128 v[88:91], v37 offset:35888
	v_mov_b32_e32 v14, v11
	s_waitcnt lgkmcnt(3)
	v_pk_fma_f32 v[96:97], v[14:15], v[76:77], v[8:9] op_sel_hi:[1,0,1]
	v_mov_b32_e32 v8, v79
	v_pk_fma_f32 v[102:103], v[14:15], v[8:9], v[102:103] op_sel_hi:[1,0,1]
	s_waitcnt lgkmcnt(2)
	v_mov_b32_e32 v8, v83
	v_pk_fma_f32 v[110:111], v[14:15], v[8:9], v[110:111] op_sel_hi:[1,0,1]
	s_waitcnt lgkmcnt(1)
	v_mov_b32_e32 v8, v87
	v_pk_fma_f32 v[112:113], v[14:15], v[84:85], v[112:113] op_sel_hi:[1,0,1]
	v_pk_fma_f32 v[84:85], v[14:15], v[84:85], v[114:115] op_sel:[0,1,0]
	v_pk_fma_f32 v[114:115], v[14:15], v[86:87], v[116:117] op_sel_hi:[1,0,1]
	v_pk_fma_f32 v[86:87], v[14:15], v[8:9], v[92:93] op_sel_hi:[1,0,1]
	s_waitcnt lgkmcnt(0)
	v_mov_b32_e32 v8, v91
	v_pk_fma_f32 v[16:17], v[14:15], v[76:77], v[16:17] op_sel:[0,1,0]
	v_pk_fma_f32 v[92:93], v[14:15], v[88:89], v[140:141] op_sel_hi:[1,0,1]
	v_pk_fma_f32 v[88:89], v[14:15], v[88:89], v[94:95] op_sel:[0,1,0]
	v_pk_fma_f32 v[94:95], v[14:15], v[90:91], v[98:99] op_sel_hi:[1,0,1]
	v_pk_fma_f32 v[90:91], v[14:15], v[8:9], v[12:13] op_sel_hi:[1,0,1]
	v_pk_fma_f32 v[100:101], v[14:15], v[78:79], v[100:101] op_sel_hi:[1,0,1]
	v_pk_fma_f32 v[104:105], v[14:15], v[80:81], v[104:105] op_sel_hi:[1,0,1]
	v_pk_fma_f32 v[106:107], v[14:15], v[80:81], v[106:107] op_sel:[0,1,0]
	v_pk_fma_f32 v[108:109], v[14:15], v[82:83], v[108:109] op_sel_hi:[1,0,1]
	ds_read_b128 v[8:11], v37 offset:56320
	ds_read_b128 v[12:15], v37 offset:56336
	ds_read_b128 v[76:79], v37 offset:56352
	ds_read_b128 v[80:83], v37 offset:56368
	v_mov_b32_e32 v98, v4
	v_mov_b32_e32 v99, v6
	s_waitcnt lgkmcnt(3)
	v_mov_b32_e32 v4, v11
	v_pk_fma_f32 v[102:103], v[98:99], v[4:5], v[102:103] op_sel_hi:[1,0,1]
	s_waitcnt lgkmcnt(2)
	v_mov_b32_e32 v4, v15
	v_pk_fma_f32 v[110:111], v[98:99], v[4:5], v[110:111] op_sel_hi:[1,0,1]
	s_waitcnt lgkmcnt(1)
	v_mov_b32_e32 v4, v79
	v_pk_fma_f32 v[16:17], v[98:99], v[8:9], v[16:17] op_sel:[0,1,0]
	v_pk_fma_f32 v[84:85], v[98:99], v[76:77], v[84:85] op_sel:[0,1,0]
	v_pk_fma_f32 v[140:141], v[98:99], v[4:5], v[86:87] op_sel_hi:[1,0,1]
	s_waitcnt lgkmcnt(0)
	v_mov_b32_e32 v4, v83
	v_pk_fma_f32 v[116:117], v[98:99], v[8:9], v[96:97] op_sel_hi:[1,0,1]
	v_pk_fma_f32 v[100:101], v[98:99], v[10:11], v[100:101] op_sel_hi:[1,0,1]
	v_pk_fma_f32 v[104:105], v[98:99], v[12:13], v[104:105] op_sel_hi:[1,0,1]
	v_pk_fma_f32 v[106:107], v[98:99], v[12:13], v[106:107] op_sel:[0,1,0]
	v_pk_fma_f32 v[108:109], v[98:99], v[14:15], v[108:109] op_sel_hi:[1,0,1]
	v_pk_fma_f32 v[112:113], v[98:99], v[76:77], v[112:113] op_sel_hi:[1,0,1]
	v_pk_fma_f32 v[114:115], v[98:99], v[78:79], v[114:115] op_sel_hi:[1,0,1]
	v_pk_fma_f32 v[142:143], v[98:99], v[80:81], v[92:93] op_sel_hi:[1,0,1]
	v_pk_fma_f32 v[144:145], v[98:99], v[80:81], v[88:89] op_sel:[0,1,0]
	v_pk_fma_f32 v[146:147], v[98:99], v[82:83], v[94:95] op_sel_hi:[1,0,1]
	v_pk_fma_f32 v[98:99], v[98:99], v[4:5], v[90:91] op_sel_hi:[1,0,1]
	v_add_u32_e32 v4, 0x12c00, v37
	v_add_u32_e32 v6, 0x12c10, v37
	ds_read_b128 v[8:11], v4
	ds_read_b128 v[80:83], v6
	v_add_u32_e32 v4, 0x12c20, v37
	v_add_u32_e32 v6, 0x12c30, v37
	ds_read_b128 v[88:91], v4
	ds_read_b128 v[94:97], v6
	v_mov_b32_e32 v6, v5
	s_waitcnt lgkmcnt(3)
	v_mov_b32_e32 v4, v11
	v_pk_fma_f32 v[76:77], v[6:7], v[4:5], v[102:103] op_sel_hi:[1,0,1]
	s_waitcnt lgkmcnt(2)
	v_pk_fma_f32 v[12:13], v[6:7], v[80:81], v[104:105] op_sel_hi:[1,0,1]
	v_pk_fma_f32 v[4:5], v[6:7], v[80:81], v[106:107] op_sel:[0,1,0]
	s_waitcnt lgkmcnt(1)
	v_mov_b32_e32 v80, v91
	v_pk_fma_f32 v[14:15], v[6:7], v[8:9], v[16:17] op_sel:[0,1,0]
	v_pk_fma_f32 v[16:17], v[6:7], v[10:11], v[100:101] op_sel_hi:[1,0,1]
	v_mov_b32_e32 v10, v83
	v_pk_fma_f32 v[92:93], v[6:7], v[88:89], v[112:113] op_sel_hi:[1,0,1]
	v_pk_fma_f32 v[86:87], v[6:7], v[88:89], v[84:85] op_sel:[0,1,0]
	v_pk_fma_f32 v[88:89], v[6:7], v[90:91], v[114:115] op_sel_hi:[1,0,1]
	v_pk_fma_f32 v[90:91], v[6:7], v[80:81], v[140:141] op_sel_hi:[1,0,1]
	s_waitcnt lgkmcnt(0)
	v_pk_fma_f32 v[84:85], v[6:7], v[94:95], v[142:143] op_sel_hi:[1,0,1]
	v_pk_fma_f32 v[80:81], v[6:7], v[94:95], v[144:145] op_sel:[0,1,0]
	v_mov_b32_e32 v94, v97
	v_pk_fma_f32 v[78:79], v[6:7], v[8:9], v[116:117] op_sel_hi:[1,0,1]
	v_pk_fma_f32 v[8:9], v[6:7], v[82:83], v[108:109] op_sel_hi:[1,0,1]
	v_pk_fma_f32 v[10:11], v[6:7], v[10:11], v[110:111] op_sel_hi:[1,0,1]
	v_pk_fma_f32 v[82:83], v[6:7], v[96:97], v[146:147] op_sel_hi:[1,0,1]
	v_pk_fma_f32 v[6:7], v[6:7], v[94:95], v[98:99] op_sel_hi:[1,0,1]
	s_nop 0
	s_nop 0
	s_nop 4
	v_permlane32_swap_b32_e32 v78, v92
	v_permlane32_swap_b32_e32 v14, v86
	v_permlane32_swap_b32_e32 v16, v88
	v_permlane32_swap_b32_e32 v76, v90
	v_permlane32_swap_b32_e32 v12, v84
	v_permlane32_swap_b32_e32 v4, v80
	v_permlane32_swap_b32_e32 v8, v82
	v_permlane32_swap_b32_e32 v10, v6
	v_add_f32_e32 v37, v92, v78
	v_add_f32_e32 v14, v86, v14
	v_add_f32_e32 v16, v88, v16
	v_add_f32_e32 v76, v90, v76
	v_add_f32_e32 v12, v84, v12
	v_add_f32_e32 v4, v80, v4
	v_add_f32_e32 v8, v82, v8
	v_add_f32_e32 v6, v6, v10
	s_nop 1
	v_permlane16_swap_b32_e32 v37, v12
	v_permlane16_swap_b32_e32 v14, v4
	v_permlane16_swap_b32_e32 v16, v8
	v_permlane16_swap_b32_e32 v76, v6
	v_add_f32_e32 v10, v12, v37
	v_add_f32_e32 v4, v4, v14
	v_add_f32_e32 v8, v8, v16
	v_add_f32_e32 v6, v6, v76
	v_cndmask_b32_e64 v12, v8, v10, s[10:11]
	v_cndmask_b32_e64 v8, v10, v8, s[10:11]
	v_cndmask_b32_e64 v10, v6, v4, s[10:11]
	v_cndmask_b32_e64 v4, v4, v6, s[10:11]
	s_nop 1
	v_add_f32_dpp v8, v8, v12 row_ror:8 row_mask:0xf bank_mask:0xf
	v_add_f32_dpp v4, v4, v10 row_ror:8 row_mask:0xf bank_mask:0xf
	v_cndmask_b32_e64 v6, v4, v8, s[12:13]
	v_cndmask_b32_e64 v4, v8, v4, s[12:13]
	s_nop 1
	v_add_f32_dpp v164, v4, v6 row_shl:4 row_mask:0xf bank_mask:0x5
	v_add_f32_dpp v164, v4, v6 row_shr:4 row_mask:0xf bank_mask:0xa
	s_nop 1
	v_add_f32_dpp v165, v164, v164 quad_perm:[2,3,0,1] row_mask:0xf bank_mask:0xf
	s_nop 1
	v_add_f32_dpp v4, v165, v165 quad_perm:[1,0,3,2] row_mask:0xf bank_mask:0xf
	v_mov_b32_e32 v164, v4
	v_mov_b32_e32 v165, v4
	s_nop 1
	v_permlane32_swap_b32_e32 v164, v165
	v_max_f32_e32 v6, v164, v165
	v_mov_b32_e32 v164, v6
	v_mov_b32_e32 v165, v6
	s_nop 1
	v_permlane16_swap_b32_e32 v164, v165
	v_max_f32_e32 v6, v164, v165
	s_nop 1
	v_max_f32_dpp v6, v6, v6 row_ror:8 row_mask:0xf bank_mask:0xf
	s_nop 1
	v_max_f32_dpp v6, v6, v6 row_half_mirror row_mask:0xf bank_mask:0xf
	v_sub_f32_e32 v4, v4, v6
	v_mul_f32_e32 v6, 0x3fb8aa3b, v4
	v_fma_f32 v8, v4, s33, -v6
	v_rndne_f32_e32 v10, v6
	v_fmac_f32_e32 v8, 0x32a5705f, v4
	v_sub_f32_e32 v6, v6, v10
	v_add_f32_e32 v6, v6, v8
	v_exp_f32_e32 v6, v6
	v_cvt_i32_f32_e32 v8, v10
	v_cmp_ngt_f32_e32 vcc, s36, v4
	v_ldexp_f32 v6, v6, v8
	s_nop 0
	v_cndmask_b32_e32 v6, 0, v6, vcc
	v_cmp_nlt_f32_e32 vcc, s53, v4
	s_nop 1
	v_cndmask_b32_e32 v4, v216, v6, vcc
	v_mov_b32_e32 v164, v4
	v_mov_b32_e32 v165, v4
	s_nop 1
	v_permlane32_swap_b32_e32 v164, v165
	v_add_f32_e32 v6, v164, v165
	v_mov_b32_e32 v164, v6
	v_mov_b32_e32 v165, v6
	s_nop 1
	v_permlane16_swap_b32_e32 v164, v165
	v_add_f32_e32 v6, v164, v165
	s_nop 1
	v_add_f32_dpp v6, v6, v6 row_ror:8 row_mask:0xf bank_mask:0xf
	s_nop 1
	v_add_f32_dpp v6, v6, v6 row_half_mirror row_mask:0xf bank_mask:0xf
	s_and_saveexec_b64 s[16:17], s[14:15]
	s_cbranch_execz .LBB0_1263
	v_div_scale_f32 v8, s[34:35], v6, v6, v4
	v_rcp_f32_e32 v10, v8
	v_div_scale_f32 v12, vcc, v4, v6, v4
	v_lshl_add_u64 v[94:95], s[62:63], 0, v[38:39]
	v_fma_f32 v14, -v8, v10, 1.0
	v_fmac_f32_e32 v10, v14, v10
	v_mul_f32_e32 v14, v12, v10
	v_fma_f32 v16, -v8, v14, v12
	v_fmac_f32_e32 v14, v16, v10
	v_fma_f32 v8, -v8, v14, v12
	v_div_fmas_f32 v8, v8, v10, v14
	v_div_fixup_f32 v4, v8, v6, v4
	global_store_dword v[94:95], v4, off
.LBB0_1263:
	s_or_b64 exec, exec, s[16:17]
	s_waitcnt lgkmcnt(0)
	s_nop 4
	v_permlane32_swap_b32_e32 v11, v7
	v_permlane32_swap_b32_e32 v79, v93
	v_permlane32_swap_b32_e32 v5, v81
	v_permlane32_swap_b32_e32 v15, v87
	v_permlane32_swap_b32_e32 v17, v89
	v_permlane32_swap_b32_e32 v77, v91
	v_permlane32_swap_b32_e32 v13, v85
	v_permlane32_swap_b32_e32 v9, v83
	v_add_f32_e32 v7, v7, v11
	v_add_f32_e32 v4, v93, v79
	v_add_f32_e32 v5, v81, v5
	v_add_f32_e32 v6, v87, v15
	v_add_f32_e32 v8, v89, v17
	v_add_f32_e32 v10, v91, v77
	v_add_f32_e32 v11, v85, v13
	v_add_f32_e32 v9, v83, v9
	s_nop 1
	v_permlane16_swap_b32_e32 v4, v11
	v_permlane16_swap_b32_e32 v6, v5
	v_permlane16_swap_b32_e32 v8, v9
	v_permlane16_swap_b32_e32 v10, v7
	v_add_f32_e32 v4, v11, v4
	v_add_f32_e32 v5, v5, v6
	v_add_f32_e32 v6, v9, v8
	v_add_f32_e32 v7, v7, v10
	v_cndmask_b32_e64 v8, v4, v6, s[10:11]
	v_cndmask_b32_e64 v4, v6, v4, s[10:11]
	v_cndmask_b32_e64 v9, v5, v7, s[10:11]
	v_cndmask_b32_e64 v5, v7, v5, s[10:11]
	s_nop 1
	v_add_f32_dpp v4, v8, v4 row_ror:8 row_mask:0xf bank_mask:0xf
	v_add_f32_dpp v5, v9, v5 row_ror:8 row_mask:0xf bank_mask:0xf
	v_cndmask_b32_e64 v6, v4, v5, s[12:13]
	v_cndmask_b32_e64 v4, v5, v4, s[12:13]
	s_nop 1
	v_add_f32_dpp v164, v6, v4 row_shl:4 row_mask:0xf bank_mask:0x5
	v_add_f32_dpp v164, v6, v4 row_shr:4 row_mask:0xf bank_mask:0xa
	s_nop 1
	v_add_f32_dpp v165, v164, v164 quad_perm:[2,3,0,1] row_mask:0xf bank_mask:0xf
	s_nop 1
	v_add_f32_dpp v4, v165, v165 quad_perm:[1,0,3,2] row_mask:0xf bank_mask:0xf
	v_mov_b32_e32 v164, v4
	v_mov_b32_e32 v165, v4
	s_nop 1
	v_permlane32_swap_b32_e32 v164, v165
	v_max_f32_e32 v5, v164, v165
	v_mov_b32_e32 v164, v5
	v_mov_b32_e32 v165, v5
	s_nop 1
	v_permlane16_swap_b32_e32 v164, v165
	v_max_f32_e32 v5, v164, v165
	s_nop 1
	v_max_f32_dpp v5, v5, v5 row_ror:8 row_mask:0xf bank_mask:0xf
	s_nop 1
	v_max_f32_dpp v5, v5, v5 row_half_mirror row_mask:0xf bank_mask:0xf
	v_sub_f32_e32 v4, v4, v5
	v_mul_f32_e32 v5, 0x3fb8aa3b, v4
	v_fma_f32 v6, v4, s33, -v5
	v_rndne_f32_e32 v7, v5
	v_fmac_f32_e32 v6, 0x32a5705f, v4
	v_sub_f32_e32 v5, v5, v7
	v_add_f32_e32 v5, v5, v6
	v_cvt_i32_f32_e32 v7, v7
	v_exp_f32_e32 v5, v5
	v_cmp_ngt_f32_e32 vcc, s36, v4
	v_ldexp_f32 v5, v5, v7
	s_nop 0
	v_cndmask_b32_e32 v5, 0, v5, vcc
	v_cmp_nlt_f32_e32 vcc, s53, v4
	s_nop 1
	v_cndmask_b32_e32 v4, v216, v5, vcc
	v_mov_b32_e32 v164, v4
	v_mov_b32_e32 v165, v4
	s_nop 1
	v_permlane32_swap_b32_e32 v164, v165
	v_add_f32_e32 v5, v164, v165
	v_mov_b32_e32 v164, v5
	v_mov_b32_e32 v165, v5
	s_nop 1
	v_permlane16_swap_b32_e32 v164, v165
	v_add_f32_e32 v5, v164, v165
	s_nop 1
	v_add_f32_dpp v5, v5, v5 row_ror:8 row_mask:0xf bank_mask:0xf
	s_nop 1
	v_add_f32_dpp v5, v5, v5 row_half_mirror row_mask:0xf bank_mask:0xf
	s_and_saveexec_b64 s[16:17], s[14:15]
	s_cbranch_execz .LBB0_1258
	v_div_scale_f32 v6, s[34:35], v5, v5, v4
	v_rcp_f32_e32 v7, v6
	v_div_scale_f32 v8, vcc, v4, v5, v4
	v_lshlrev_b64 v[2:3], 6, v[2:3]
	v_fma_f32 v9, -v6, v7, 1.0
	v_fmac_f32_e32 v7, v9, v7
	v_mul_f32_e32 v9, v8, v7
	v_fma_f32 v10, -v6, v9, v8
	v_fmac_f32_e32 v9, v10, v7
	v_fma_f32 v6, -v6, v9, v8
	v_div_fmas_f32 v6, v6, v7, v9
	v_div_fixup_f32 v4, v6, v5, v4
	v_lshl_add_u64 v[2:3], v[24:25], 0, v[2:3]
	global_store_dword v[2:3], v4, off
	s_branch .LBB0_1258
